# FIRST kernel: waves 4-7 branch around the per-tile f_bond row gathers and index load that only waves 0-3 consume (they duplicated the same addresses)
# baseline (speedup 1.0000x reference)
_Z10mp2_kernelILb0ELi1EEvPKDF16_PDF16_PKiPKfPKDv8_DF16_S6_S6_ii:
	v_lshrrev_b32_e32 v152, 6, v0
	s_load_dwordx4 s[8:11], s[0:1], 0x20
	s_load_dwordx2 s[4:5], s[0:1], 0x30
	v_readfirstlane_b32 s3, v152
	s_lshr_b32 s24, s3, 2
	s_mul_i32 s6, s3, 29
	s_ashr_i32 s7, s6, 31
	s_lshl_b64 s[6:7], s[6:7], 10
	v_and_b32_e32 v1, 63, v0
	s_waitcnt lgkmcnt(0)
	s_add_u32 s6, s8, s6
	s_addc_u32 s7, s9, s7
	v_lshlrev_b32_e32 v150, 4, v1
	v_mov_b32_e32 v151, 0
	v_lshl_add_u64 v[34:35], s[6:7], 0, v[150:151]
	s_movk_i32 s8, 0x1000
	v_add_co_u32_e32 v94, vcc, s8, v34
	s_movk_i32 s8, 0x2000
	s_nop 0
	v_addc_co_u32_e32 v95, vcc, 0, v35, vcc
	v_add_co_u32_e32 v118, vcc, s8, v34
	s_movk_i32 s8, 0x3000
	s_nop 0
	v_addc_co_u32_e32 v119, vcc, 0, v35, vcc
	v_add_co_u32_e32 v96, vcc, s8, v34
	s_movk_i32 s8, 0x4000
	s_nop 0
	v_addc_co_u32_e32 v97, vcc, 0, v35, vcc
	v_add_co_u32_e32 v98, vcc, s8, v34
	s_movk_i32 s8, 0x5000
	s_nop 0
	v_addc_co_u32_e32 v99, vcc, 0, v35, vcc
	v_add_co_u32_e32 v100, vcc, s8, v34
	s_movk_i32 s8, 0x6000
	s_nop 0
	v_addc_co_u32_e32 v101, vcc, 0, v35, vcc
	v_add_co_u32_e32 v102, vcc, s8, v34
	global_load_dwordx4 v[2:5], v[94:95], off offset:1024
	global_load_dwordx4 v[6:9], v[94:95], off offset:2048
	v_addc_co_u32_e32 v103, vcc, 0, v35, vcc
	v_add_co_u32_e32 v120, vcc, 0x7000, v34
	global_load_dwordx4 v[10:13], v[118:119], off
	global_load_dwordx4 v[14:17], v[118:119], off offset:1024
	global_load_dwordx4 v[18:21], v[96:97], off offset:3072
	global_load_dwordx4 v[22:25], v[98:99], off offset:1024
	global_load_dwordx4 v[26:29], v[118:119], off offset:2048
	global_load_dwordx4 v[30:33], v[118:119], off offset:3072
	v_addc_co_u32_e32 v121, vcc, 0, v35, vcc
	global_load_dwordx4 v[34:37], v[98:99], off offset:2048
	global_load_dwordx4 v[38:41], v[98:99], off offset:3072
	global_load_dwordx4 v[42:45], v[96:97], off offset:1024
	global_load_dwordx4 v[46:49], v[96:97], off offset:2048
	global_load_dwordx4 v[50:53], v[94:95], off offset:3072
	global_load_dwordx4 v[54:57], v[96:97], off
	global_load_dwordx4 v[58:61], v[100:101], off offset:-4096
	global_load_dwordx4 v[62:65], v[100:101], off
	global_load_dwordx4 v[66:69], v[100:101], off offset:1024
	global_load_dwordx4 v[70:73], v[100:101], off offset:2048
	global_load_dwordx4 v[74:77], v[100:101], off offset:3072
	global_load_dwordx4 v[78:81], v[102:103], off offset:2048
	global_load_dwordx4 v[82:85], v[102:103], off offset:3072
	global_load_dwordx4 v[86:89], v[102:103], off offset:1024
	global_load_dwordx4 v[90:93], v[102:103], off
	global_load_dwordx4 v[94:97], v[120:121], off
	global_load_dwordx4 v[98:101], v150, s[6:7]
	s_nop 0
	global_load_dwordx4 v[102:105], v[118:119], off offset:-4096
	global_load_dwordx4 v[106:109], v150, s[6:7] offset:3072
	global_load_dwordx4 v[110:113], v150, s[6:7] offset:1024
	global_load_dwordx4 v[114:117], v150, s[6:7] offset:2048
	s_movk_i32 s6, 0x80
	v_cmp_gt_u32_e32 vcc, s6, v0
	s_and_saveexec_b64 s[6:7], vcc
	s_cbranch_execz .LBB6_2

.LBB6_16:
	v_or_b32_e32 v0, s23, v201
	v_cndmask_b32_e64 v0, v217, v0, s[4:5]
	ds_read_b128 v[134:137], v196 offset:0
	s_waitcnt lgkmcnt(4)
	s_nop 0
	v_mfma_f32_16x16x32_f16 v[138:141], v[114:117], v[150:153], v[166:169]
	ds_read_b128 v[142:145], v196 offset:0x1000
	s_waitcnt lgkmcnt(4)
	s_nop 0
	v_mfma_f32_16x16x32_f16 v[146:149], v[114:117], v[154:157], v[170:173]
	ds_read_b128 v[150:153], v196 offset:0x2000
	s_waitcnt lgkmcnt(4)
	s_nop 0
	v_mfma_f32_16x16x32_f16 v[154:157], v[114:117], v[158:161], v[174:177]
	ds_read_b128 v[158:161], v196 offset:0x3000
	s_waitcnt lgkmcnt(4)
	s_nop 0
	v_mfma_f32_16x16x32_f16 v[162:165], v[114:117], v[162:165], v[178:181]
	ds_read_b128 v[166:169], v0 offset:0
	s_waitcnt lgkmcnt(4)
	s_nop 0
	v_mfma_f32_16x16x32_f16 v[134:137], v[106:109], v[134:137], v[138:141]
	ds_read_b128 v[138:141], v0 offset:0x100
	s_waitcnt lgkmcnt(4)
	s_nop 0
	v_mfma_f32_16x16x32_f16 v[142:145], v[106:109], v[142:145], v[146:149]
	ds_read_b128 v[146:149], v0 offset:0x200
	s_waitcnt lgkmcnt(4)
	s_nop 0
	v_mfma_f32_16x16x32_f16 v[150:153], v[106:109], v[150:153], v[154:157]
	ds_read_b128 v[154:157], v0 offset:0x300
	s_waitcnt lgkmcnt(4)
	s_nop 0
	v_mfma_f32_16x16x32_f16 v[158:161], v[106:109], v[158:161], v[162:165]
	s_waitcnt lgkmcnt(3)
	s_nop 0
	v_mfma_f32_16x16x32_f16 v[134:137], v[102:105], v[166:169], v[134:137]
	s_waitcnt lgkmcnt(2)
	s_nop 0
	v_mfma_f32_16x16x32_f16 v[138:141], v[102:105], v[138:141], v[142:145]
	s_waitcnt lgkmcnt(1)
	s_nop 0
	v_mfma_f32_16x16x32_f16 v[142:145], v[102:105], v[146:149], v[150:153]
	s_waitcnt lgkmcnt(0)
	s_nop 0
	v_mfma_f32_16x16x32_f16 v[146:149], v[102:105], v[154:157], v[158:161]
	s_nop 1
	v_cvt_pk_f16_f32 v1, v136, v137
	v_pk_max_f16 v1, v1, 0
	v_cvt_pk_f16_f32 v0, v134, v135
	v_pk_max_f16 v0, v0, 0
	v_cvt_pk_f16_f32 v135, v140, v141
	v_pk_max_f16 v135, v135, 0
	v_cvt_pk_f16_f32 v134, v138, v139
	v_pk_max_f16 v134, v134, 0
	ds_write2st64_b64 v216, v[0:1], v[134:135] offset1:8
	v_cvt_pk_f16_f32 v1, v144, v145
	v_pk_max_f16 v1, v1, 0
	v_cvt_pk_f16_f32 v0, v142, v143
	v_pk_max_f16 v0, v0, 0
	v_cvt_pk_f16_f32 v135, v148, v149
	v_pk_max_f16 v135, v135, 0
	v_cvt_pk_f16_f32 v134, v146, v147
	v_pk_max_f16 v134, v134, 0
	ds_write2st64_b64 v216, v[0:1], v[134:135] offset0:16 offset1:24
	s_waitcnt lgkmcnt(0)
	s_barrier
	ds_read_b128 v[134:137], v197 offset:0
	ds_read_b128 v[138:141], v198 offset:0
	ds_read_b128 v[142:145], v199 offset:0
	ds_read_b128 v[146:149], v200 offset:0
	ds_read_b128 v[150:153], v206 offset:0
	v_add_u32_e32 v0, s16, v213
	s_waitcnt lgkmcnt(4)
	v_min_i32_e32 v0, s11, v0
	v_mfma_f32_16x16x32_f16 v[154:157], v[2:5], v[134:137], v[118:121]
	v_cndmask_b32_e64 v0, v190, v0, s[8:9]
	v_ashrrev_i32_e32 v1, 31, v0
	ds_read_b128 v[162:165], v207 offset:0
	v_mfma_f32_16x16x32_f16 v[158:161], v[42:45], v[134:137], v[122:125]
	s_waitcnt lgkmcnt(4)
	v_lshlrev_b64 v[0:1], 5, v[0:1]
	v_lshl_add_u64 v[0:1], s[14:15], 0, v[0:1]
	v_mfma_f32_16x16x32_f16 v[134:137], v[66:69], v[134:137], v[126:129]
	v_lshl_add_u64 v[170:171], v[0:1], 0, 16
	v_mfma_f32_16x16x32_f16 v[154:157], v[6:9], v[138:141], v[154:157]
	v_mfma_f32_16x16x32_f16 v[158:161], v[46:49], v[138:141], v[158:161]
	v_mfma_f32_16x16x32_f16 v[166:169], v[70:73], v[138:141], v[134:137]
	s_cmp_lg_u32 s24, 0
	s_cbranch_scc1 .Lfirst_norows
	global_load_dwordx4 v[138:141], v[0:1], off
	global_load_dwordx4 v[134:137], v[170:171], off
.Lfirst_norows:
	ds_read_b128 v[170:173], v208 offset:0
	s_waitcnt lgkmcnt(4)
	v_add_u32_e32 v0, s16, v212
	v_mfma_f32_16x16x32_f16 v[154:157], v[50:53], v[142:145], v[154:157]
	v_min_i32_e32 v0, s11, v0
	v_mad_i64_i32 v[0:1], s[2:3], v0, 12, s[12:13]
	v_mfma_f32_16x16x32_f16 v[158:161], v[18:21], v[142:145], v[158:161]
	v_lshl_add_u64 v[0:1], v[0:1], 0, v[186:187]
	s_cmp_lg_u32 s24, 0
	s_cbranch_scc1 .Lfirst_nogidx
	global_load_dword v190, v[0:1], off
.Lfirst_nogidx:
	v_mfma_f32_16x16x32_f16 v[142:145], v[74:77], v[142:145], v[166:169]
	ds_read_b128 v[166:169], v209 offset:0
	s_waitcnt lgkmcnt(4)
	s_nop 0
	v_mfma_f32_16x16x32_f16 v[154:157], v[10:13], v[146:149], v[154:157]
	v_mfma_f32_16x16x32_f16 v[158:161], v[58:61], v[146:149], v[158:161]
	v_mfma_f32_16x16x32_f16 v[146:149], v[90:93], v[146:149], v[142:145]
	ds_read_b128 v[142:145], v197 offset:0x1000
	s_waitcnt lgkmcnt(4)
	ds_read_b128 v[174:177], v198 offset:0x1000
	s_waitcnt lgkmcnt(4)
	s_nop 0
	v_mfma_f32_16x16x32_f16 v[154:157], v[14:17], v[150:153], v[154:157]
	v_mfma_f32_16x16x32_f16 v[158:161], v[22:25], v[150:153], v[158:161]
	v_mfma_f32_16x16x32_f16 v[150:153], v[86:89], v[150:153], v[130:133]
	v_mfma_f32_16x16x32_f16 v[154:157], v[26:29], v[162:165], v[154:157]
	v_mfma_f32_16x16x32_f16 v[158:161], v[34:37], v[162:165], v[158:161]
	v_mfma_f32_16x16x32_f16 v[150:153], v[78:81], v[162:165], v[150:153]
	ds_read_b128 v[162:165], v199 offset:0x1000
	s_waitcnt lgkmcnt(4)
	s_nop 0
	v_mfma_f32_16x16x32_f16 v[154:157], v[30:33], v[170:173], v[154:157]
	v_mfma_f32_16x16x32_f16 v[158:161], v[38:41], v[170:173], v[158:161]
	v_mfma_f32_16x16x32_f16 v[150:153], v[82:85], v[170:173], v[150:153]
	ds_read_b128 v[170:173], v200 offset:0x1000
	s_waitcnt lgkmcnt(4)
	s_nop 0
	v_mfma_f32_16x16x32_f16 v[154:157], v[54:57], v[166:169], v[154:157]
	v_mfma_f32_16x16x32_f16 v[158:161], v[62:65], v[166:169], v[158:161]
	v_mfma_f32_16x16x32_f16 v[150:153], v[94:97], v[166:169], v[150:153]
	s_nop 5
	v_exp_f32_e32 v154, v154
	v_exp_f32_e32 v158, v158
	ds_read_b64 v[0:1], v204 offset:0
	ds_read_b128 v[166:169], v206 offset:0x1000
	v_add_f32_e32 v154, 1.0, v154
	v_rcp_f32_e32 v154, v154
	v_add_f32_e32 v158, 1.0, v158
	s_waitcnt lgkmcnt(5)
	ds_read_b128 v[220:223], v207 offset:0x1000
	v_fma_f32 v146, v154, v150, v146
	v_exp_f32_e32 v146, v146
	v_exp_f32_e32 v154, v155
	v_rcp_f32_e32 v150, v158
	v_mfma_f32_16x16x32_f16 v[178:181], v[2:5], v[142:145], v[118:121]
	v_add_f32_e32 v146, 1.0, v146
	v_add_f32_e32 v154, 1.0, v154
	v_rcp_f32_e32 v146, v146
	v_rcp_f32_e32 v154, v154
	v_mfma_f32_16x16x32_f16 v[182:185], v[42:45], v[142:145], v[122:125]
	s_waitcnt lgkmcnt(5)
	v_fma_f32 v146, v146, -2.0, 1.0
	v_fma_f32 v147, v154, v151, v147
	v_mfma_f32_16x16x32_f16 v[142:145], v[66:69], v[142:145], v[126:129]
	v_fma_f32 v146, -v150, v146, v146
	v_exp_f32_e32 v147, v147
	s_waitcnt lgkmcnt(2)
	v_mfma_f32_16x16x32_f16 v[178:181], v[6:9], v[174:177], v[178:181]
	v_fma_mixlo_f16 v146, v150, v0, v146 op_sel_hi:[0,1,0]
	v_exp_f32_e32 v150, v159
	v_add_f32_e32 v147, 1.0, v147
	v_mfma_f32_16x16x32_f16 v[182:185], v[46:49], v[174:177], v[182:185]
	v_rcp_f32_e32 v151, v147
	v_add_f32_e32 v150, 1.0, v150
	v_rcp_f32_e32 v150, v150
	v_mfma_f32_16x16x32_f16 v[142:145], v[70:73], v[174:177], v[142:145]
	ds_read_b128 v[174:177], v208 offset:0x1000
	s_waitcnt lgkmcnt(5)
	v_cmp_eq_u32_e32 vcc, s16, v211
	v_mfma_f32_16x16x32_f16 v[178:181], v[50:53], v[162:165], v[178:181]
	v_add_u32_e32 v218, v193, v210
	v_cndmask_b32_e64 v189, v146, 0, vcc
	v_add_u32_e32 v188, 0x1000, v218
	v_mfma_f32_16x16x32_f16 v[182:185], v[18:21], v[162:165], v[182:185]
	v_mfma_f32_16x16x32_f16 v[142:145], v[74:77], v[162:165], v[142:145]
	ds_read_b128 v[162:165], v209 offset:0x1000
	s_waitcnt lgkmcnt(5)
	s_nop 0
	v_mfma_f32_16x16x32_f16 v[178:181], v[10:13], v[170:173], v[178:181]
	v_mfma_f32_16x16x32_f16 v[182:185], v[58:61], v[170:173], v[182:185]
	v_mfma_f32_16x16x32_f16 v[144:147], v[90:93], v[170:173], v[142:145]
	s_nop 3
	v_fma_f32 v142, v151, -2.0, 1.0
	v_fma_f32 v142, -v150, v142, v142
	v_fma_mixlo_f16 v0, v150, v0, v142 op_sel:[0,1,0] op_sel_hi:[0,1,0]
	v_cndmask_b32_e64 v0, v0, 0, vcc
	v_exp_f32_e32 v142, v156
	ds_read_b128 v[170:173], v197 offset:0x2000
	s_waitcnt lgkmcnt(4)
	v_exp_f32_e32 v143, v160
	v_add_f32_e32 v142, 1.0, v142
	v_rcp_f32_e32 v142, v142
	v_mfma_f32_16x16x32_f16 v[182:185], v[22:25], v[166:169], v[182:185]
	ds_read_b128 v[224:227], v198 offset:0x2000
	s_waitcnt lgkmcnt(4)
	v_fma_f32 v142, v142, v152, v148
	v_exp_f32_e32 v148, v157
	v_mfma_f32_16x16x32_f16 v[178:181], v[14:17], v[166:169], v[178:181]
	v_exp_f32_e32 v142, v142
	v_add_f32_e32 v143, 1.0, v143
	v_add_f32_e32 v148, 1.0, v148
	v_rcp_f32_e32 v148, v148
	v_mfma_f32_16x16x32_f16 v[166:169], v[86:89], v[166:169], v[130:133]
	v_add_f32_e32 v142, 1.0, v142
	v_rcp_f32_e32 v142, v142
	v_rcp_f32_e32 v143, v143
	v_mfma_f32_16x16x32_f16 v[182:185], v[34:37], v[220:223], v[182:185]
	v_fmac_f32_e32 v149, v148, v153
	v_exp_f32_e32 v150, v161
	v_fma_f32 v142, v142, -2.0, 1.0
	v_mfma_f32_16x16x32_f16 v[178:181], v[26:29], v[220:223], v[178:181]
	v_fma_f32 v142, -v143, v142, v142
	v_fma_mixlo_f16 v142, v143, v1, v142 op_sel_hi:[0,1,0]
	v_add_f32_e32 v143, 1.0, v150
	v_mfma_f32_16x16x32_f16 v[154:157], v[78:81], v[220:223], v[166:169]
	ds_read_b128 v[166:169], v199 offset:0x2000
	s_waitcnt lgkmcnt(4)
	v_rcp_f32_e32 v143, v143
	v_mfma_f32_16x16x32_f16 v[158:161], v[38:41], v[174:177], v[182:185]
	v_cndmask_b32_e64 v142, v142, 0, vcc
	v_pack_b32_f16 v0, v189, v0
	s_nop 0
	v_exp_f32_e32 v182, v149
	v_mfma_f32_16x16x32_f16 v[178:181], v[30:33], v[174:177], v[178:181]
	v_mfma_f32_16x16x32_f16 v[148:151], v[82:85], v[174:177], v[154:157]
	ds_read_b128 v[152:155], v200 offset:0x2000
	s_waitcnt lgkmcnt(4)
	s_nop 0
	v_mfma_f32_16x16x32_f16 v[174:177], v[54:57], v[162:165], v[178:181]
	s_nop 0
	v_add_f32_e32 v156, 1.0, v182
	s_nop 2
	v_rcp_f32_e32 v178, v156
	v_mfma_f32_16x16x32_f16 v[156:159], v[62:65], v[162:165], v[158:161]
	s_nop 2
	v_fma_f32 v160, v178, -2.0, 1.0
	v_fma_f32 v160, -v143, v160, v160
	v_mfma_f32_16x16x32_f16 v[148:151], v[94:97], v[162:165], v[148:151]
	v_fma_mixlo_f16 v1, v143, v1, v160 op_sel:[0,1,0] op_sel_hi:[0,1,0]
	v_cndmask_b32_e64 v1, v1, 0, vcc
	v_pack_b32_f16 v1, v142, v1
	global_store_dwordx2 v188, v[0:1], s[0:1] nt
	v_exp_f32_e32 v142, v174
	v_exp_f32_e32 v143, v156
	ds_read_b64 v[0:1], v204 offset:0x1000
	ds_read_b128 v[160:163], v206 offset:0x2000
	v_add_f32_e32 v142, 1.0, v142
	v_rcp_f32_e32 v142, v142
	s_waitcnt lgkmcnt(5)
	v_add_f32_e32 v143, 1.0, v143
	v_mfma_f32_16x16x32_f16 v[178:181], v[2:5], v[170:173], v[118:121]
	v_fma_f32 v142, v142, v148, v144
	v_exp_f32_e32 v144, v175
	v_exp_f32_e32 v142, v142
	v_mfma_f32_16x16x32_f16 v[182:185], v[42:45], v[170:173], v[122:125]
	v_rcp_f32_e32 v143, v143
	v_add_f32_e32 v144, 1.0, v144
	v_add_f32_e32 v142, 1.0, v142
	v_mfma_f32_16x16x32_f16 v[170:173], v[66:69], v[170:173], v[126:129]
	v_rcp_f32_e32 v144, v144
	v_rcp_f32_e32 v142, v142
	ds_read_b128 v[220:223], v207 offset:0x2000
	s_waitcnt lgkmcnt(5)
	v_fma_f32 v148, v144, v149, v145
	v_mfma_f32_16x16x32_f16 v[178:181], v[6:9], v[224:227], v[178:181]
	v_fma_f32 v142, v142, -2.0, 1.0
	v_exp_f32_e32 v148, v148
	v_fma_f32 v142, -v143, v142, v142
	v_mfma_f32_16x16x32_f16 v[182:185], v[46:49], v[224:227], v[182:185]
	v_exp_f32_e32 v149, v157
	s_waitcnt lgkmcnt(2)
	v_add_f32_e32 v148, 1.0, v148
	v_mfma_f32_16x16x32_f16 v[170:173], v[70:73], v[224:227], v[170:173]
	ds_read_b128 v[224:227], v208 offset:0x2000
	s_waitcnt lgkmcnt(5)
	v_fma_mixlo_f16 v188, v143, v0, v142 op_sel_hi:[0,1,0]
	v_mfma_f32_16x16x32_f16 v[178:181], v[50:53], v[166:169], v[178:181]
	v_rcp_f32_e32 v148, v148
	v_add_f32_e32 v149, 1.0, v149
	v_rcp_f32_e32 v232, v149
	v_mfma_f32_16x16x32_f16 v[182:185], v[18:21], v[166:169], v[182:185]
	v_fma_f32 v148, v148, -2.0, 1.0
	v_add_u32_e32 v219, 0x2000, v218
	v_fma_f32 v233, -v232, v148, v148
	v_mfma_f32_16x16x32_f16 v[142:145], v[74:77], v[166:169], v[170:173]
	ds_read_b128 v[170:173], v209 offset:0x2000
	s_waitcnt lgkmcnt(5)
	s_nop 0
	v_mfma_f32_16x16x32_f16 v[164:167], v[10:13], v[152:155], v[178:181]
	v_mfma_f32_16x16x32_f16 v[178:181], v[58:61], v[152:155], v[182:185]
	v_mfma_f32_16x16x32_f16 v[142:145], v[90:93], v[152:155], v[142:145]
	v_exp_f32_e32 v148, v176
	v_exp_f32_e32 v149, v158
	ds_read_b128 v[228:231], v197 offset:0x3000
	s_waitcnt lgkmcnt(4)
	v_add_f32_e32 v148, 1.0, v148
	v_rcp_f32_e32 v148, v148
	v_mfma_f32_16x16x32_f16 v[152:155], v[14:17], v[160:163], v[164:167]
	v_fma_mixhi_f16 v188, v232, v0, v233 op_sel:[0,1,0] op_sel_hi:[0,1,0]
	v_fma_f32 v146, v148, v150, v146
	v_add_f32_e32 v148, 1.0, v149
	v_exp_f32_e32 v149, v177
	v_mfma_f32_16x16x32_f16 v[166:169], v[22:25], v[160:163], v[178:181]
	v_exp_f32_e32 v146, v146
	v_exp_f32_e32 v150, v159
	v_add_f32_e32 v149, 1.0, v149
	v_rcp_f32_e32 v149, v149
	v_mfma_f32_16x16x32_f16 v[178:181], v[86:89], v[160:163], v[130:133]
	ds_read_b128 v[162:165], v198 offset:0x3000
	s_waitcnt lgkmcnt(4)
	v_fmac_f32_e32 v147, v149, v151
	v_exp_f32_e32 v147, v147
	v_add_f32_e32 v146, 1.0, v146
	v_mfma_f32_16x16x32_f16 v[152:155], v[26:29], v[220:223], v[152:155]
	v_rcp_f32_e32 v146, v146
	v_add_f32_e32 v147, 1.0, v147
	v_rcp_f32_e32 v148, v148
	v_mfma_f32_16x16x32_f16 v[182:185], v[34:37], v[220:223], v[166:169]
	v_add_f32_e32 v150, 1.0, v150
	v_rcp_f32_e32 v147, v147
	v_rcp_f32_e32 v150, v150
	v_mfma_f32_16x16x32_f16 v[174:177], v[78:81], v[220:223], v[178:181]
	ds_read_b128 v[166:169], v199 offset:0x3000
	s_waitcnt lgkmcnt(4)
	v_fma_f32 v146, v146, -2.0, 1.0
	v_mfma_f32_16x16x32_f16 v[152:155], v[30:33], v[224:227], v[152:155]
	v_fma_f32 v146, -v148, v146, v146
	v_fma_f32 v151, v147, -2.0, 1.0
	v_fma_mixlo_f16 v189, v148, v1, v146 op_sel_hi:[0,1,0]
	v_mfma_f32_16x16x32_f16 v[178:181], v[38:41], v[224:227], v[182:185]
	v_fma_f32 v151, -v150, v151, v151
	ds_read_b128 v[158:161], v200 offset:0x3000
	s_waitcnt lgkmcnt(4)
	v_mfma_f32_16x16x32_f16 v[174:177], v[82:85], v[224:227], v[174:177]
	v_fma_mixhi_f16 v189, v150, v1, v151 op_sel:[0,1,0] op_sel_hi:[0,1,0]
	global_store_dwordx2 v219, v[188:189], s[0:1] nt
	v_mfma_f32_16x16x32_f16 v[154:157], v[54:57], v[170:173], v[152:155]
	v_mfma_f32_16x16x32_f16 v[146:149], v[62:65], v[170:173], v[178:181]
	v_mfma_f32_16x16x32_f16 v[150:153], v[94:97], v[170:173], v[174:177]
	ds_read_b64 v[188:189], v204 offset:0x2000
	ds_read_b64 v[0:1], v204 offset:0x3000
	ds_read_b128 v[170:173], v206 offset:0x3000
	s_waitcnt lgkmcnt(6)
	s_waitcnt vmcnt(2)
	s_nop 0
	v_mfma_f32_16x16x32_f16 v[182:185], v[2:5], v[228:231], v[118:121]
	v_mfma_f32_16x16x32_f16 v[174:177], v[42:45], v[228:231], v[122:125]
	v_mfma_f32_16x16x32_f16 v[178:181], v[66:69], v[228:231], v[126:129]
	s_and_saveexec_b64 s[2:3], s[6:7]
	s_cbranch_execz .LBB6_13
	s_xor_b32 s23, s23, 0x1000
	v_cvt_pk_f16_f32 v221, v140, v141
	v_cvt_pk_f16_f32 v220, v138, v139
	v_cvt_pk_f16_f32 v223, v136, v137
	v_cvt_pk_f16_f32 v222, v134, v135
	v_add_u32_e32 v134, s23, v205
	ds_write_b128 v134, v[220:223] offset:49152
	s_branch .LBB6_13

	.amdhsa_kernel _Z10mp2_kernelILb0ELi1EEvPKDF16_PDF16_PKiPKfPKDv8_DF16_S6_S6_ii
		.amdhsa_group_segment_fixed_size 0
		.amdhsa_private_segment_fixed_size 0
		.amdhsa_kernarg_size 320
		.amdhsa_user_sgpr_count 2
		.amdhsa_user_sgpr_dispatch_ptr 0
		.amdhsa_user_sgpr_queue_ptr 0
		.amdhsa_user_sgpr_kernarg_segment_ptr 1
		.amdhsa_user_sgpr_dispatch_id 0
		.amdhsa_user_sgpr_kernarg_preload_length 0
		.amdhsa_user_sgpr_kernarg_preload_offset 0
		.amdhsa_user_sgpr_private_segment_size 0
		.amdhsa_uses_dynamic_stack 0
		.amdhsa_enable_private_segment 0
		.amdhsa_system_sgpr_workgroup_id_x 1
		.amdhsa_system_sgpr_workgroup_id_y 0
		.amdhsa_system_sgpr_workgroup_id_z 0
		.amdhsa_system_sgpr_workgroup_info 0
		.amdhsa_system_vgpr_workitem_id 0
		.amdhsa_next_free_vgpr 234
		.amdhsa_next_free_sgpr 26
		.amdhsa_accum_offset 236
		.amdhsa_reserve_vcc 1
		.amdhsa_float_round_mode_32 0
		.amdhsa_float_round_mode_16_64 0
		.amdhsa_float_denorm_mode_32 3
		.amdhsa_float_denorm_mode_16_64 3
		.amdhsa_dx10_clamp 1
		.amdhsa_ieee_mode 1
		.amdhsa_fp16_overflow 0
		.amdhsa_tg_split 0
		.amdhsa_exception_fp_ieee_invalid_op 0
		.amdhsa_exception_fp_denorm_src 0
		.amdhsa_exception_fp_ieee_div_zero 0
		.amdhsa_exception_fp_ieee_overflow 0
		.amdhsa_exception_fp_ieee_underflow 0
		.amdhsa_exception_fp_ieee_inexact 0
		.amdhsa_exception_int_div_zero 0
	.end_amdhsa_kernel

amdhsa.kernels:
  - .agpr_count:     0
    .args:
      - .actual_access:  write_only
        .address_space:  global
        .offset:         0
        .size:           8
        .value_kind:     global_buffer
      - .actual_access:  read_only
        .address_space:  global
        .offset:         8
        .size:           8
        .value_kind:     global_buffer
      - .actual_access:  read_only
        .address_space:  global
        .offset:         16
        .size:           8
        .value_kind:     global_buffer
      - .actual_access:  read_only
        .address_space:  global
        .offset:         24
        .size:           8
        .value_kind:     global_buffer
      - .actual_access:  read_only
        .address_space:  global
        .offset:         32
        .size:           8
        .value_kind:     global_buffer
      - .actual_access:  read_only
        .address_space:  global
        .offset:         40
        .size:           8
        .value_kind:     global_buffer
      - .actual_access:  read_only
        .address_space:  global
        .offset:         48
        .size:           8
        .value_kind:     global_buffer
      - .actual_access:  read_only
        .address_space:  global
        .offset:         56
        .size:           8
        .value_kind:     global_buffer
      - .actual_access:  read_only
        .address_space:  global
        .offset:         64
        .size:           8
        .value_kind:     global_buffer
      - .actual_access:  read_only
        .address_space:  global
        .offset:         72
        .size:           8
        .value_kind:     global_buffer
    .group_segment_fixed_size: 0
    .kernarg_segment_align: 8
    .kernarg_segment_size: 80
    .language:       OpenCL C
    .language_version:
      - 2
      - 0
    .max_flat_workgroup_size: 64
    .name:           _Z11prep_kernelPDv8_DF16_PKfS2_S2_S2_S2_S2_S2_S2_S2_
    .private_segment_fixed_size: 0
    .sgpr_count:     20
    .sgpr_spill_count: 0
    .symbol:         _Z11prep_kernelPDv8_DF16_PKfS2_S2_S2_S2_S2_S2_S2_S2_.kd
    .uniform_work_group_size: 1
    .uses_dynamic_stack: false
    .vgpr_count:     18
    .vgpr_spill_count: 0
    .wavefront_size: 64
  - .agpr_count:     0
    .args:
      - .actual_access:  read_only
        .address_space:  global
        .offset:         0
        .size:           8
        .value_kind:     global_buffer
      - .actual_access:  read_only
        .address_space:  global
        .offset:         8
        .size:           8
        .value_kind:     global_buffer
      - .actual_access:  write_only
        .address_space:  global
        .offset:         16
        .size:           8
        .value_kind:     global_buffer
    .group_segment_fixed_size: 0
    .kernarg_segment_align: 8
    .kernarg_segment_size: 24
    .language:       OpenCL C
    .language_version:
      - 2
      - 0
    .max_flat_workgroup_size: 256
    .name:           _Z11init_kernelPKfS0_PDF16_
    .private_segment_fixed_size: 0
    .sgpr_count:     16
    .sgpr_spill_count: 0
    .symbol:         _Z11init_kernelPKfS0_PDF16_.kd
    .uniform_work_group_size: 1
    .uses_dynamic_stack: false
    .vgpr_count:     118
    .vgpr_spill_count: 0
    .wavefront_size: 64
  - .agpr_count:     0
    .args:
      - .actual_access:  read_only
        .address_space:  global
        .offset:         0
        .size:           8
        .value_kind:     global_buffer
      - .actual_access:  write_only
        .address_space:  global
        .offset:         8
        .size:           8
        .value_kind:     global_buffer
      - .actual_access:  read_only
        .address_space:  global
        .offset:         16
        .size:           8
        .value_kind:     global_buffer
      - .actual_access:  read_only
        .address_space:  global
        .offset:         24
        .size:           8
        .value_kind:     global_buffer
      - .actual_access:  read_only
        .address_space:  global
        .offset:         32
        .size:           8
        .value_kind:     global_buffer
      - .actual_access:  read_only
        .address_space:  global
        .offset:         40
        .size:           8
        .value_kind:     global_buffer
      - .actual_access:  read_only
        .address_space:  global
        .offset:         48
        .size:           8
        .value_kind:     global_buffer
      - .offset:         56
        .size:           4
        .value_kind:     by_value
      - .offset:         64
        .size:           4
        .value_kind:     hidden_block_count_x
      - .offset:         68
        .size:           4
        .value_kind:     hidden_block_count_y
      - .offset:         72
        .size:           4
        .value_kind:     hidden_block_count_z
      - .offset:         76
        .size:           2
        .value_kind:     hidden_group_size_x
      - .offset:         78
        .size:           2
        .value_kind:     hidden_group_size_y
      - .offset:         80
        .size:           2
        .value_kind:     hidden_group_size_z
      - .offset:         82
        .size:           2
        .value_kind:     hidden_remainder_x
      - .offset:         84
        .size:           2
        .value_kind:     hidden_remainder_y
      - .offset:         86
        .size:           2
        .value_kind:     hidden_remainder_z
      - .offset:         104
        .size:           8
        .value_kind:     hidden_global_offset_x
      - .offset:         112
        .size:           8
        .value_kind:     hidden_global_offset_y
      - .offset:         120
        .size:           8
        .value_kind:     hidden_global_offset_z
      - .offset:         128
        .size:           2
        .value_kind:     hidden_grid_dims
      - .offset:         184
        .size:           4
        .value_kind:     hidden_dynamic_lds_size
    .group_segment_fixed_size: 0
    .kernarg_segment_align: 8
    .kernarg_segment_size: 320
    .language:       OpenCL C
    .language_version:
      - 2
      - 0
    .max_flat_workgroup_size: 512
    .name:           _Z12xproj_kernelPKDF16_PDF16_PKDv8_DF16_PKfS6_S6_S6_i
    .private_segment_fixed_size: 0
    .sgpr_count:     30
    .sgpr_spill_count: 0
    .symbol:         _Z12xproj_kernelPKDF16_PDF16_PKDv8_DF16_PKfS6_S6_S6_i.kd
    .uniform_work_group_size: 1
    .uses_dynamic_stack: false
    .vgpr_count:     16
    .vgpr_spill_count: 0
    .wavefront_size: 64
  - .agpr_count:     0
    .args:
      - .actual_access:  read_only
        .address_space:  global
        .offset:         0
        .size:           8
        .value_kind:     global_buffer
      - .actual_access:  read_only
        .address_space:  global
        .offset:         8
        .size:           8
        .value_kind:     global_buffer
      - .actual_access:  write_only
        .address_space:  global
        .offset:         16
        .size:           8
        .value_kind:     global_buffer
    .group_segment_fixed_size: 5120
    .kernarg_segment_align: 8
    .kernarg_segment_size: 24
    .language:       OpenCL C
    .language_version:
      - 2
      - 0
    .max_flat_workgroup_size: 1024
    .name:           _Z11lstm_kernelPKDF16_PKDv8_DF16_Pf
    .private_segment_fixed_size: 0
    .sgpr_count:     18
    .sgpr_spill_count: 0
    .symbol:         _Z11lstm_kernelPKDF16_PKDv8_DF16_Pf.kd
    .uniform_work_group_size: 1
    .uses_dynamic_stack: false
    .vgpr_count:     52
    .vgpr_spill_count: 0
    .wavefront_size: 64
  - .agpr_count:     0
    .args:
      - .actual_access:  read_only
        .address_space:  global
        .offset:         0
        .size:           8
        .value_kind:     global_buffer
      - .actual_access:  read_only
        .address_space:  global
        .offset:         8
        .size:           8
        .value_kind:     global_buffer
      - .actual_access:  write_only
        .address_space:  global
        .offset:         16
        .size:           8
        .value_kind:     global_buffer
    .group_segment_fixed_size: 36096
    .kernarg_segment_align: 8
    .kernarg_segment_size: 24
    .language:       OpenCL C
    .language_version:
      - 2
      - 0
    .max_flat_workgroup_size: 256
    .name:           _Z12lstm2_kernelPKDF16_PKDv8_DF16_Pf
    .private_segment_fixed_size: 0
    .sgpr_count:     38
    .sgpr_spill_count: 0
    .symbol:         _Z12lstm2_kernelPKDF16_PKDv8_DF16_Pf.kd
    .uniform_work_group_size: 1
    .uses_dynamic_stack: false
    .vgpr_count:     252
    .vgpr_spill_count: 0
    .wavefront_size: 64
  - .agpr_count:     0
    .args:
      - .address_space:  global
        .offset:         0
        .size:           8
        .value_kind:     global_buffer
      - .actual_access:  write_only
        .address_space:  global
        .offset:         8
        .size:           8
        .value_kind:     global_buffer
      - .address_space:  global
        .offset:         16
        .size:           8
        .value_kind:     global_buffer
      - .address_space:  global
        .offset:         24
        .size:           8
        .value_kind:     global_buffer
      - .actual_access:  read_only
        .address_space:  global
        .offset:         32
        .size:           8
        .value_kind:     global_buffer
      - .actual_access:  read_only
        .address_space:  global
        .offset:         40
        .size:           8
        .value_kind:     global_buffer
      - .actual_access:  read_only
        .address_space:  global
        .offset:         48
        .size:           8
        .value_kind:     global_buffer
      - .offset:         56
        .size:           4
        .value_kind:     by_value
      - .offset:         60
        .size:           4
        .value_kind:     by_value
      - .offset:         64
        .size:           4
        .value_kind:     hidden_block_count_x
      - .offset:         68
        .size:           4
        .value_kind:     hidden_block_count_y
      - .offset:         72
        .size:           4
        .value_kind:     hidden_block_count_z
      - .offset:         76
        .size:           2
        .value_kind:     hidden_group_size_x
      - .offset:         78
        .size:           2
        .value_kind:     hidden_group_size_y
      - .offset:         80
        .size:           2
        .value_kind:     hidden_group_size_z
      - .offset:         82
        .size:           2
        .value_kind:     hidden_remainder_x
      - .offset:         84
        .size:           2
        .value_kind:     hidden_remainder_y
      - .offset:         86
        .size:           2
        .value_kind:     hidden_remainder_z
      - .offset:         104
        .size:           8
        .value_kind:     hidden_global_offset_x
      - .offset:         112
        .size:           8
        .value_kind:     hidden_global_offset_y
      - .offset:         120
        .size:           8
        .value_kind:     hidden_global_offset_z
      - .offset:         128
        .size:           2
        .value_kind:     hidden_grid_dims
      - .offset:         184
        .size:           4
        .value_kind:     hidden_dynamic_lds_size
    .group_segment_fixed_size: 0
    .kernarg_segment_align: 8
    .kernarg_segment_size: 320
    .language:       OpenCL C
    .language_version:
      - 2
      - 0
    .max_flat_workgroup_size: 512
    .name:           _Z10mp2_kernelILb0ELi0EEvPKDF16_PDF16_PKiPKfPKDv8_DF16_S6_S6_ii
    .private_segment_fixed_size: 0
    .sgpr_count:     54
    .sgpr_spill_count: 0
    .symbol:         _Z10mp2_kernelILb0ELi0EEvPKDF16_PDF16_PKiPKfPKDv8_DF16_S6_S6_ii.kd
    .uniform_work_group_size: 1
    .uses_dynamic_stack: false
    .vgpr_count:     244
    .vgpr_spill_count: 0
    .wavefront_size: 64
  - .agpr_count:     0
    .args:
      - .actual_access:  read_only
        .address_space:  global
        .offset:         0
        .size:           8
        .value_kind:     global_buffer
      - .actual_access:  write_only
        .address_space:  global
        .offset:         8
        .size:           8
        .value_kind:     global_buffer
      - .address_space:  global
        .offset:         16
        .size:           8
        .value_kind:     global_buffer
      - .address_space:  global
        .offset:         24
        .size:           8
        .value_kind:     global_buffer
      - .actual_access:  read_only
        .address_space:  global
        .offset:         32
        .size:           8
        .value_kind:     global_buffer
      - .actual_access:  read_only
        .address_space:  global
        .offset:         40
        .size:           8
        .value_kind:     global_buffer
      - .actual_access:  read_only
        .address_space:  global
        .offset:         48
        .size:           8
        .value_kind:     global_buffer
      - .offset:         56
        .size:           4
        .value_kind:     by_value
      - .offset:         60
        .size:           4
        .value_kind:     by_value
      - .offset:         64
        .size:           4
        .value_kind:     hidden_block_count_x
      - .offset:         68
        .size:           4
        .value_kind:     hidden_block_count_y
      - .offset:         72
        .size:           4
        .value_kind:     hidden_block_count_z
      - .offset:         76
        .size:           2
        .value_kind:     hidden_group_size_x
      - .offset:         78
        .size:           2
        .value_kind:     hidden_group_size_y
      - .offset:         80
        .size:           2
        .value_kind:     hidden_group_size_z
      - .offset:         82
        .size:           2
        .value_kind:     hidden_remainder_x
      - .offset:         84
        .size:           2
        .value_kind:     hidden_remainder_y
      - .offset:         86
        .size:           2
        .value_kind:     hidden_remainder_z
      - .offset:         104
        .size:           8
        .value_kind:     hidden_global_offset_x
      - .offset:         112
        .size:           8
        .value_kind:     hidden_global_offset_y
      - .offset:         120
        .size:           8
        .value_kind:     hidden_global_offset_z
      - .offset:         128
        .size:           2
        .value_kind:     hidden_grid_dims
      - .offset:         184
        .size:           4
        .value_kind:     hidden_dynamic_lds_size
    .group_segment_fixed_size: 0
    .kernarg_segment_align: 8
    .kernarg_segment_size: 320
    .language:       OpenCL C
    .language_version:
      - 2
      - 0
    .max_flat_workgroup_size: 512
    .name:           _Z10mp2_kernelILb0ELi1EEvPKDF16_PDF16_PKiPKfPKDv8_DF16_S6_S6_ii
    .private_segment_fixed_size: 0
    .sgpr_count:     32
    .sgpr_spill_count: 0
    .symbol:         _Z10mp2_kernelILb0ELi1EEvPKDF16_PDF16_PKiPKfPKDv8_DF16_S6_S6_ii.kd
    .uniform_work_group_size: 1
    .uses_dynamic_stack: false
    .vgpr_count:     234
    .vgpr_spill_count: 0
    .wavefront_size: 64
  - .agpr_count:     0
    .args:
      - .address_space:  global
        .offset:         0
        .size:           8
        .value_kind:     global_buffer
      - .actual_access:  write_only
        .address_space:  global
        .offset:         8
        .size:           8
        .value_kind:     global_buffer
      - .actual_access:  read_only
        .address_space:  global
        .offset:         16
        .size:           8
        .value_kind:     global_buffer
      - .actual_access:  read_only
        .address_space:  global
        .offset:         24
        .size:           8
        .value_kind:     global_buffer
      - .actual_access:  read_only
        .address_space:  global
        .offset:         32
        .size:           8
        .value_kind:     global_buffer
      - .actual_access:  read_only
        .address_space:  global
        .offset:         40
        .size:           8
        .value_kind:     global_buffer
      - .actual_access:  read_only
        .address_space:  global
        .offset:         48
        .size:           8
        .value_kind:     global_buffer
      - .offset:         56
        .size:           4
        .value_kind:     by_value
      - .offset:         60
        .size:           4
        .value_kind:     by_value
      - .offset:         64
        .size:           4
        .value_kind:     hidden_block_count_x
      - .offset:         68
        .size:           4
        .value_kind:     hidden_block_count_y
      - .offset:         72
        .size:           4
        .value_kind:     hidden_block_count_z
      - .offset:         76
        .size:           2
        .value_kind:     hidden_group_size_x
      - .offset:         78
        .size:           2
        .value_kind:     hidden_group_size_y
      - .offset:         80
        .size:           2
        .value_kind:     hidden_group_size_z
      - .offset:         82
        .size:           2
        .value_kind:     hidden_remainder_x
      - .offset:         84
        .size:           2
        .value_kind:     hidden_remainder_y
      - .offset:         86
        .size:           2
        .value_kind:     hidden_remainder_z
      - .offset:         104
        .size:           8
        .value_kind:     hidden_global_offset_x
      - .offset:         112
        .size:           8
        .value_kind:     hidden_global_offset_y
      - .offset:         120
        .size:           8
        .value_kind:     hidden_global_offset_z
      - .offset:         128
        .size:           2
        .value_kind:     hidden_grid_dims
      - .offset:         184
        .size:           4
        .value_kind:     hidden_dynamic_lds_size
    .group_segment_fixed_size: 0
    .kernarg_segment_align: 8
    .kernarg_segment_size: 320
    .language:       OpenCL C
    .language_version:
      - 2
      - 0
    .max_flat_workgroup_size: 512
    .name:           _Z9mp_kernelILi1EEvPKDF16_PDF16_PKiPKfPKDv8_DF16_S6_S6_ii
    .private_segment_fixed_size: 0
    .sgpr_count:     46
    .sgpr_spill_count: 0
    .symbol:         _Z9mp_kernelILi1EEvPKDF16_PDF16_PKiPKfPKDv8_DF16_S6_S6_ii.kd
    .uniform_work_group_size: 1
    .uses_dynamic_stack: false
    .vgpr_count:     70
    .vgpr_spill_count: 0
    .wavefront_size: 64
  - .agpr_count:     0
    .args:
      - .address_space:  global
        .offset:         0
        .size:           8
        .value_kind:     global_buffer
      - .actual_access:  write_only
        .address_space:  global
        .offset:         8
        .size:           8
        .value_kind:     global_buffer
      - .address_space:  global
        .offset:         16
        .size:           8
        .value_kind:     global_buffer
      - .address_space:  global
        .offset:         24
        .size:           8
        .value_kind:     global_buffer
      - .actual_access:  read_only
        .address_space:  global
        .offset:         32
        .size:           8
        .value_kind:     global_buffer
      - .actual_access:  read_only
        .address_space:  global
        .offset:         40
        .size:           8
        .value_kind:     global_buffer
      - .actual_access:  read_only
        .address_space:  global
        .offset:         48
        .size:           8
        .value_kind:     global_buffer
      - .offset:         56
        .size:           4
        .value_kind:     by_value
      - .offset:         60
        .size:           4
        .value_kind:     by_value
      - .offset:         64
        .size:           4
        .value_kind:     hidden_block_count_x
      - .offset:         68
        .size:           4
        .value_kind:     hidden_block_count_y
      - .offset:         72
        .size:           4
        .value_kind:     hidden_block_count_z
      - .offset:         76
        .size:           2
        .value_kind:     hidden_group_size_x
      - .offset:         78
        .size:           2
        .value_kind:     hidden_group_size_y
      - .offset:         80
        .size:           2
        .value_kind:     hidden_group_size_z
      - .offset:         82
        .size:           2
        .value_kind:     hidden_remainder_x
      - .offset:         84
        .size:           2
        .value_kind:     hidden_remainder_y
      - .offset:         86
        .size:           2
        .value_kind:     hidden_remainder_z
      - .offset:         104
        .size:           8
        .value_kind:     hidden_global_offset_x
      - .offset:         112
        .size:           8
        .value_kind:     hidden_global_offset_y
      - .offset:         120
        .size:           8
        .value_kind:     hidden_global_offset_z
      - .offset:         128
        .size:           2
        .value_kind:     hidden_grid_dims
      - .offset:         184
        .size:           4
        .value_kind:     hidden_dynamic_lds_size
    .group_segment_fixed_size: 0
    .kernarg_segment_align: 8
    .kernarg_segment_size: 320
    .language:       OpenCL C
    .language_version:
      - 2
      - 0
    .max_flat_workgroup_size: 512
    .name:           _Z10mp2_kernelILb0ELi2EEvPKDF16_PDF16_PKiPKfPKDv8_DF16_S6_S6_ii
    .private_segment_fixed_size: 0
    .sgpr_count:     34
    .sgpr_spill_count: 0
    .symbol:         _Z10mp2_kernelILb0ELi2EEvPKDF16_PDF16_PKiPKfPKDv8_DF16_S6_S6_ii.kd
    .uniform_work_group_size: 1
    .uses_dynamic_stack: false
    .vgpr_count:     99
    .vgpr_spill_count: 0
    .wavefront_size: 64
